# baseline (speedup 1.0000x reference)
_Z15k_scatter_gemm1PKiS0_PiPjPyPKfPK6__halfS5_S5_PS6_PfSA_:
	s_cmpk_gt_u32 s2, 0x186
	s_mov_b64 s[4:5], -1
	s_cbranch_scc0 .LBB1_22
	s_load_dwordx2 s[26:27], s[0:1], 0x28
	s_load_dwordx2 s[10:11], s[0:1], 0x30
	s_load_dwordx4 s[28:31], s[0:1], 0x38
	v_lshlrev_b32_e32 v92, 4, v0
	v_add_u32_e32 v93, 0x1000, v92
	v_add_u32_e32 v94, 0x2000, v92
	v_add_u32_e32 v95, 0x3000, v92
	v_add_u32_e32 v96, 0x4000, v92
	v_add_u32_e32 v97, 0x5000, v92
	v_add_u32_e32 v98, 0x6000, v92
	v_add_u32_e32 v99, 0x7000, v92
	v_add_u32_e32 v100, 0x8000, v92
	v_lshlrev_b32_e32 v101, 2, v0
	s_movk_i32 s3, 0x80
	v_cmp_gt_u32_e64 s[8:9], s3, v0
	s_waitcnt lgkmcnt(0)
	global_load_dwordx4 v[104:107], v92, s[10:11]
	global_load_dwordx4 v[108:111], v93, s[10:11]
	global_load_dwordx4 v[112:115], v94, s[10:11]
	global_load_dwordx4 v[116:119], v95, s[10:11]
	global_load_dwordx4 v[120:123], v96, s[10:11]
	global_load_dwordx4 v[124:127], v97, s[10:11]
	global_load_dwordx4 v[128:131], v98, s[10:11]
	global_load_dwordx4 v[132:135], v99, s[10:11]
	s_and_saveexec_b64 s[4:5], s[8:9]
	global_load_dwordx4 v[136:139], v100, s[10:11]
	global_load_dword v140, v101, s[28:29]
	global_load_dword v141, v101, s[30:31]
	s_mov_b64 exec, s[4:5]
	s_lshl_b32 s3, s2, 2
	v_lshrrev_b32_e32 v14, 6, v0
	s_add_i32 s4, s3, 0xfffff9e4
	v_or_b32_e32 v2, s4, v14
	s_movk_i32 s4, 0xc35
	v_cmp_gt_i32_e32 vcc, s4, v2
	v_and_b32_e32 v1, 15, v0
	v_and_b32_e32 v66, 48, v0
	v_mov_b32_e32 v67, 0
	s_and_saveexec_b64 s[6:7], vcc
	s_cbranch_execz .Lg1_noval
	v_lshl_or_b32 v2, v2, 4, v1
	v_ashrrev_i32_e32 v3, 31, v2
	v_lshlrev_b64 v[2:3], 9, v[2:3]
	v_lshl_add_u64 v[2:3], s[26:27], 0, v[2:3]
	v_lshl_add_u64 v[16:17], v[2:3], 0, v[66:67]
	global_load_dwordx4 v[38:41], v[16:17], off offset:448
	global_load_dwordx4 v[34:37], v[16:17], off offset:384
	global_load_dwordx4 v[46:49], v[16:17], off offset:320
	global_load_dwordx4 v[42:45], v[16:17], off offset:256
	global_load_dwordx4 v[6:9], v[16:17], off offset:192
	global_load_dwordx4 v[18:21], v[16:17], off offset:128
	global_load_dwordx4 v[2:5], v[16:17], off offset:64
	global_load_dwordx4 v[10:13], v[16:17], off
	s_mov_b64 exec, s[6:7]
	s_waitcnt vmcnt(8)
	s_branch .Lg1_stage

.Lg1_stage:
	ds_write_b128 v92, v[104:107]
	ds_write_b128 v92, v[108:111] offset:4096
	ds_write_b128 v92, v[112:115] offset:8192
	ds_write_b128 v92, v[116:119] offset:12288
	ds_write_b128 v92, v[120:123] offset:16384
	ds_write_b128 v92, v[124:127] offset:20480
	ds_write_b128 v92, v[128:131] offset:24576
	ds_write_b128 v92, v[132:135] offset:28672
	s_and_saveexec_b64 s[4:5], s[8:9]
	ds_write_b128 v92, v[136:139] offset:32768
	ds_write2st64_b32 v101, v140, v141 offset0:204 offset1:206
	s_mov_b64 exec, s[4:5]
	s_waitcnt lgkmcnt(0)
	s_barrier
	s_and_saveexec_b64 s[6:7], vcc
	s_cbranch_execz .LBB1_21
	s_load_dwordx2 s[8:9], s[0:1], 0x58
	s_load_dwordx2 s[10:11], s[0:1], 0x48
	v_and_b32_e32 v15, 63, v0
	v_lshl_add_u64 v[68:69], s[26:27], 0, v[66:67]
	s_movk_i32 s4, 0x1100
	v_cmp_gt_u32_e32 vcc, 16, v15
	v_mul_u32_u24_e32 v15, 0x110, v1
	v_mul_u32_u24_e32 v17, 0x1100, v14
	v_mad_u32_u24 v22, v14, s4, v15
	v_lshlrev_b32_e32 v16, 4, v1
	v_add_u32_e32 v25, s3, v14
	v_lshlrev_b32_e32 v14, 4, v14
	v_bfe_u32 v80, v0, 4, 2
	v_or_b32_e32 v24, v17, v16
	v_mov_b32_e32 v17, v67
	v_lshl_or_b32 v82, s2, 6, v14
	v_mbcnt_lo_u32_b32 v14, -1, 0
	s_waitcnt lgkmcnt(0)
	v_lshl_add_u64 v[70:71], s[10:11], 0, v[16:17]
	v_or_b32_e32 v17, 4, v80
	v_mbcnt_hi_u32_b32 v84, -1, v14
	v_lshlrev_b32_e32 v23, 3, v80
	v_mul_u32_u24_e32 v16, 0x110, v80
	v_mul_u32_u24_e32 v17, 0x110, v17
	v_and_b32_e32 v14, 64, v84
	v_subrev_u32_e32 v67, 56, v25
	v_or_b32_e32 v81, 0xffff9e40, v1
	s_mov_b64 s[10:11], 0
	s_movk_i32 s3, 0x651
	v_add_u32_e32 v83, v66, v15
	v_xor_b32_e32 v85, 16, v84
	v_add_u32_e32 v86, 64, v14
	v_xor_b32_e32 v87, 32, v84
	v_add_u32_e32 v88, v22, v23
	v_add_u32_e32 v89, v24, v16
	v_add_u32_e32 v90, v24, v17
	s_movk_i32 s12, 0x650
	s_waitcnt vmcnt(0)
	s_branch .LBB1_19

_Z12k_fine_gemm1PKjPKyPKiPiS5_S5_S5_PKfPK6__halfS7_S7_PS8_PfSC_:
	s_cmpk_gt_u32 s2, 0x186
	s_mov_b64 s[4:5], -1
	s_cbranch_scc0 .LBB2_22
	s_load_dwordx2 s[26:27], s[0:1], 0x38
	s_load_dwordx2 s[10:11], s[0:1], 0x40
	s_load_dwordx4 s[28:31], s[0:1], 0x48
	v_lshlrev_b32_e32 v92, 4, v0
	v_add_u32_e32 v93, 0x1000, v92
	v_add_u32_e32 v94, 0x2000, v92
	v_add_u32_e32 v95, 0x3000, v92
	v_add_u32_e32 v96, 0x4000, v92
	v_add_u32_e32 v97, 0x5000, v92
	v_add_u32_e32 v98, 0x6000, v92
	v_add_u32_e32 v99, 0x7000, v92
	v_add_u32_e32 v100, 0x8000, v92
	v_lshlrev_b32_e32 v101, 2, v0
	s_movk_i32 s3, 0x80
	v_cmp_gt_u32_e64 s[8:9], s3, v0
	s_waitcnt lgkmcnt(0)
	global_load_dwordx4 v[104:107], v92, s[10:11]
	global_load_dwordx4 v[108:111], v93, s[10:11]
	global_load_dwordx4 v[112:115], v94, s[10:11]
	global_load_dwordx4 v[116:119], v95, s[10:11]
	global_load_dwordx4 v[120:123], v96, s[10:11]
	global_load_dwordx4 v[124:127], v97, s[10:11]
	global_load_dwordx4 v[128:131], v98, s[10:11]
	global_load_dwordx4 v[132:135], v99, s[10:11]
	s_and_saveexec_b64 s[4:5], s[8:9]
	global_load_dwordx4 v[136:139], v100, s[10:11]
	global_load_dword v140, v101, s[28:29]
	global_load_dword v141, v101, s[30:31]
	s_mov_b64 exec, s[4:5]
	s_lshl_b32 s3, s2, 2
	v_lshrrev_b32_e32 v14, 6, v0
	s_addk_i32 s3, 0x619
	v_add_u32_e32 v1, s3, v14
	s_movk_i32 s3, 0x186a
	v_cmp_gt_i32_e32 vcc, s3, v1
	v_and_b32_e32 v80, 15, v0
	v_and_b32_e32 v66, 48, v0
	v_mov_b32_e32 v67, 0
	s_and_saveexec_b64 s[6:7], vcc
	s_cbranch_execz .Lg2_noval
	v_lshl_or_b32 v2, v1, 4, v80
	v_ashrrev_i32_e32 v3, 31, v2
	v_lshlrev_b64 v[2:3], 9, v[2:3]
	v_lshl_add_u64 v[2:3], s[26:27], 0, v[2:3]
	v_lshl_add_u64 v[16:17], v[2:3], 0, v[66:67]
	global_load_dwordx4 v[38:41], v[16:17], off offset:448
	global_load_dwordx4 v[34:37], v[16:17], off offset:384
	global_load_dwordx4 v[26:29], v[16:17], off offset:320
	global_load_dwordx4 v[30:33], v[16:17], off offset:256
	global_load_dwordx4 v[6:9], v[16:17], off offset:192
	global_load_dwordx4 v[18:21], v[16:17], off offset:128
	global_load_dwordx4 v[2:5], v[16:17], off offset:64
	global_load_dwordx4 v[10:13], v[16:17], off
	s_mov_b64 exec, s[6:7]
	s_waitcnt vmcnt(8)
	s_branch .Lg2_stage

.Lg2_stage:
	ds_write_b128 v92, v[104:107]
	ds_write_b128 v92, v[108:111] offset:4096
	ds_write_b128 v92, v[112:115] offset:8192
	ds_write_b128 v92, v[116:119] offset:12288
	ds_write_b128 v92, v[120:123] offset:16384
	ds_write_b128 v92, v[124:127] offset:20480
	ds_write_b128 v92, v[128:131] offset:24576
	ds_write_b128 v92, v[132:135] offset:28672
	s_and_saveexec_b64 s[4:5], s[8:9]
	ds_write_b128 v92, v[136:139] offset:32768
	ds_write2st64_b32 v101, v140, v141 offset0:204 offset1:206
	s_mov_b64 exec, s[4:5]
	s_waitcnt lgkmcnt(0)
	s_barrier
	s_and_saveexec_b64 s[6:7], vcc
	s_cbranch_execz .LBB2_21
	s_load_dwordx2 s[8:9], s[0:1], 0x68
	s_load_dwordx2 s[10:11], s[0:1], 0x58
	v_and_b32_e32 v15, 63, v0
	s_movk_i32 s3, 0x1100
	v_cmp_gt_u32_e32 vcc, 16, v15
	v_mul_u32_u24_e32 v15, 0x110, v80
	v_mul_u32_u24_e32 v17, 0x1100, v14
	v_mad_u32_u24 v22, v14, s3, v15
	v_lshlrev_b32_e32 v16, 4, v80
	v_lshlrev_b32_e32 v14, 4, v14
	v_bfe_u32 v81, v0, 4, 2
	v_or_b32_e32 v24, v17, v16
	v_mov_b32_e32 v17, v67
	v_lshl_or_b32 v82, s2, 6, v14
	v_mbcnt_lo_u32_b32 v14, -1, 0
	s_waitcnt lgkmcnt(0)
	v_lshl_add_u64 v[70:71], s[10:11], 0, v[16:17]
	v_or_b32_e32 v17, 4, v81
	v_mbcnt_hi_u32_b32 v84, -1, v14
	v_lshlrev_b32_e32 v23, 3, v81
	v_mul_u32_u24_e32 v16, 0x110, v81
	v_mul_u32_u24_e32 v17, 0x110, v17
	v_and_b32_e32 v14, 64, v84
	v_lshl_add_u64 v[68:69], s[26:27], 0, v[66:67]
	v_or_b32_e32 v67, 0x6190, v80
	s_mov_b64 s[10:11], 0
	s_movk_i32 s3, 0x1285
	s_movk_i32 s14, 0x1286
	v_add_u32_e32 v83, v66, v15
	v_xor_b32_e32 v85, 16, v84
	v_add_u32_e32 v86, 64, v14
	v_xor_b32_e32 v87, 32, v84
	v_add_u32_e32 v88, v22, v23
	v_add_u32_e32 v89, v24, v16
	v_add_u32_e32 v90, v24, v17
	s_waitcnt vmcnt(0)
	s_branch .LBB2_19
